# combine phase: loads software-pipelined across loop iterations (next token pair prefetched into fresh registers)
# baseline (speedup 1.0000x reference)
; #define PE WSP(int, W_PE)
; #define PR WSP(int, W_PR)
; #define YB WSP(unsigned char, W_YB)
; __device__ __forceinline__ void combine_phase(LAS unsigned char* lds, const bf16_t* X, bf16_t* Xo, const unsigned char* __restrict__ YB, const float* __restrict__ mod_l, const int* __restrict__ cnt_l, ...
;     ...
;             g2[q] = *(const f32x4*)(mod_l + (size_t)b * 6 * D + 5 * D + k0 + 4 * q) * (1.f / Y8_SCALE);
;             const f32x4 g = *(const f32x4*)(gain + k0 + 4 * q);
;             if (mod_n) { const f32x4 sc = *(const f32x4*)(mod_n + (size_t)b * 6 * D + D + k0 + 4 * q); sh[q] = *(const f32x4*)(mod_n + (size_t)b * 6 * D + k0 + 4 * q); gn[q] = g * (sc + 1.f); }
;             else { gn[q] = g; sh[q] = (f32x4){0.f, 0.f, 0.f, 0.f}; }
;         }
;         int rowv = 0;
;         if (lane < 32) { const int e = PE[t0 * 4 + lane], rk = PR[t0 * 4 + lane]; rowv = offp[e] + rk; }
; #pragma unroll 2
;         for (int i = 0; i < 8; ++i) {
;             const int t = t0 + i;
;             u32x4 yv[4];
; #pragma unroll
;             for (int k = 0; k < 4; ++k) { const int row = __builtin_amdgcn_readlane(rowv, i * 4 + k); yv[k] = __builtin_nontemporal_load((const u32x4*)(YB + (size_t)row * D + k0)); }
;             const u32x4 x0 = *(const u32x4*)(X + (size_t)t * D + k0), x1 = *(const u32x4*)(X + (size_t)t * D + k0 + 8);
.LBB0_1505:
	s_or_b64 exec, exec, s[18:19]
	s_mov_b32 s18, 0x3d800000
	s_waitcnt vmcnt(0)
	v_pk_mul_f32 v[82:83], v[66:67], s[18:19] op_sel_hi:[1,0]
	v_pk_mul_f32 v[84:85], v[64:65], s[18:19] op_sel_hi:[1,0]
	v_pk_mul_f32 v[86:87], v[62:63], s[18:19] op_sel_hi:[1,0]
	v_pk_mul_f32 v[88:89], v[60:61], s[18:19] op_sel_hi:[1,0]
	v_pk_mul_f32 v[90:91], v[58:59], s[18:19] op_sel_hi:[1,0]
	v_pk_mul_f32 v[92:93], v[56:57], s[18:19] op_sel_hi:[1,0]
	v_pk_mul_f32 v[94:95], v[54:55], s[18:19] op_sel_hi:[1,0]
	v_pk_mul_f32 v[96:97], v[52:53], s[18:19] op_sel_hi:[1,0]
	s_mov_b32 s21, 7
	v_mov_b32_e32 v98, v108
	s_add_i32 vcc_lo, s21, -7
	v_readlane_b32 vcc_lo, v109, vcc_lo
	s_ashr_i32 vcc_hi, vcc_lo, 31
	s_lshl_b64 vcc, vcc, 10
	v_lshl_add_u64 v[210:211], v[72:73], 0, vcc
	global_load_dwordx4 v[210:213], v[210:211], off nt
	s_add_i32 vcc_lo, s21, -6
	v_readlane_b32 vcc_lo, v109, vcc_lo
	s_ashr_i32 vcc_hi, vcc_lo, 31
	s_lshl_b64 vcc, vcc, 10
	v_lshl_add_u64 v[214:215], v[72:73], 0, vcc
	global_load_dwordx4 v[214:217], v[214:215], off nt
	s_add_i32 vcc_lo, s21, -5
	v_readlane_b32 vcc_lo, v109, vcc_lo
	s_ashr_i32 vcc_hi, vcc_lo, 31
	s_lshl_b64 vcc, vcc, 10
	v_lshl_add_u64 v[218:219], v[72:73], 0, vcc
	global_load_dwordx4 v[218:221], v[218:219], off nt
	s_add_i32 vcc_lo, s21, -4
	v_readlane_b32 vcc_lo, v109, vcc_lo
	s_ashr_i32 vcc_hi, vcc_lo, 31
	s_lshl_b64 vcc, vcc, 10
	v_lshl_add_u64 v[222:223], v[72:73], 0, vcc
	global_load_dwordx4 v[222:225], v[222:223], off nt
	v_mov_b32_e32 v236, v98
	v_ashrrev_i32_e32 v237, 31, v236
	v_lshlrev_b64 v[236:237], 11, v[236:237]
	v_lshl_add_u64 v[234:235], v[74:75], 0, v[236:237]
	global_load_dwordx4 v[226:229], v[234:235], off offset:16
	global_load_dwordx4 v[230:233], v[234:235], off
	s_add_i32 vcc_lo, s21, -3
	v_readlane_b32 vcc_lo, v109, vcc_lo
	s_ashr_i32 vcc_hi, vcc_lo, 31
	s_lshl_b64 vcc, vcc, 10
	v_lshl_add_u64 v[182:183], v[72:73], 0, vcc
	global_load_dwordx4 v[182:185], v[182:183], off nt
	s_add_i32 vcc_lo, s21, -2
	v_readlane_b32 vcc_lo, v109, vcc_lo
	s_ashr_i32 vcc_hi, vcc_lo, 31
	s_lshl_b64 vcc, vcc, 10
	v_lshl_add_u64 v[186:187], v[72:73], 0, vcc
	global_load_dwordx4 v[186:189], v[186:187], off nt
	s_add_i32 vcc_lo, s21, -1
	v_readlane_b32 vcc_lo, v109, vcc_lo
	s_ashr_i32 vcc_hi, vcc_lo, 31
	s_lshl_b64 vcc, vcc, 10
	v_lshl_add_u64 v[190:191], v[72:73], 0, vcc
	global_load_dwordx4 v[190:193], v[190:191], off nt
	s_mov_b32 vcc_lo, s21
	v_readlane_b32 vcc_lo, v109, vcc_lo
	s_ashr_i32 vcc_hi, vcc_lo, 31
	s_lshl_b64 vcc, vcc, 10
	v_lshl_add_u64 v[194:195], v[72:73], 0, vcc
	global_load_dwordx4 v[194:197], v[194:195], off nt
	v_add_u32_e32 v208, 1, v98
	v_ashrrev_i32_e32 v209, 31, v208
	v_lshlrev_b64 v[208:209], 11, v[208:209]
	v_lshl_add_u64 v[206:207], v[74:75], 0, v[208:209]
	global_load_dwordx4 v[198:201], v[206:207], off offset:16
	global_load_dwordx4 v[202:205], v[206:207], off
	s_branch .LBB0_1508

; #define YB WSP(unsigned char, W_YB)
; __device__ __forceinline__ void combine_phase(LAS unsigned char* lds, const bf16_t* X, bf16_t* Xo, const unsigned char* __restrict__ YB, const float* __restrict__ mod_l, const int* __restrict__ cnt_l, ...
;     ...
;         for (int i = 0; i < 8; ++i) {
;             const int t = t0 + i;
;             u32x4 yv[4];
; #pragma unroll
;             for (int k = 0; k < 4; ++k) { const int row = __builtin_amdgcn_readlane(rowv, i * 4 + k); yv[k] = __builtin_nontemporal_load((const u32x4*)(YB + (size_t)row * D + k0)); }
;             const u32x4 x0 = *(const u32x4*)(X + (size_t)t * D + k0), x1 = *(const u32x4*)(X + (size_t)t * D + k0 + 8);
;             f32x4 v[4]; float ss = 0.f;
; #pragma unroll
;             for (int q = 0; q < 4; ++q) {
;                 f32x4 a = (f32x4){0.f, 0.f, 0.f, 0.f};
; #pragma unroll
;                 for (int k = 0; k < 4; ++k) { const unsigned w = q == 0 ? yv[k].x : q == 1 ? yv[k].y : q == 2 ? yv[k].z : yv[k].w;
;                     const f32x2_t lo = __builtin_amdgcn_cvt_pk_f32_fp8((int)w, false), hi = __builtin_amdgcn_cvt_pk_f32_fp8((int)w, true);
;                     a[0] += lo.x; a[1] += lo.y; a[2] += hi.x; a[3] += hi.y; }
;                 const u32x4 xq = (q >> 1) ? x1 : x0; const unsigned xa = (q & 1) ? xq.z : xq.x, xb = (q & 1) ? xq.w : xq.y;
;                 v[q] = (f32x4){__uint_as_float(xa << 16), __uint_as_float(xa & 0xffff0000u), __uint_as_float(xb << 16), __uint_as_float(xb & 0xffff0000u)} + g2[q] * a;
;                 ss += v[q][0] * v[q][0] + v[q][1] * v[q][1] + v[q][2] * v[q][2] + v[q][3] * v[q][3];
;             }
.LBB0_1508:
	v_ashrrev_i32_e32 v99, 31, v98
	s_mov_b32 s18, 0x358637bd
	v_lshlrev_b64 v[100:101], 10, v[98:99]
	s_waitcnt vmcnt(11)
	v_cvt_pk_f32_fp8_e32 v[102:103], v210
	v_cvt_pk_f32_fp8_sdwa v[104:105], v210 src0_sel:WORD_1
	s_waitcnt vmcnt(10)
	v_cvt_pk_f32_fp8_e32 v[114:115], v214
	v_cvt_pk_f32_fp8_sdwa v[116:117], v214 src0_sel:WORD_1
	s_waitcnt vmcnt(9)
	v_cvt_pk_f32_fp8_e32 v[118:119], v218
	v_cvt_pk_f32_fp8_sdwa v[120:121], v218 src0_sel:WORD_1
	s_waitcnt vmcnt(8)
	v_cvt_pk_f32_fp8_e32 v[122:123], v222
	v_cvt_pk_f32_fp8_sdwa v[124:125], v222 src0_sel:WORD_1
	v_pk_add_f32 v[104:105], v[104:105], 0 op_sel_hi:[1,0]
	v_pk_add_f32 v[102:103], v[102:103], 0 op_sel_hi:[1,0]
	v_pk_add_f32 v[104:105], v[104:105], v[116:117]
	v_pk_add_f32 v[102:103], v[102:103], v[114:115]
	v_pk_add_f32 v[104:105], v[104:105], v[120:121]
	v_pk_add_f32 v[102:103], v[102:103], v[118:119]
	v_cvt_pk_f32_fp8_e32 v[116:117], v219
	v_pk_add_f32 v[114:115], v[102:103], v[122:123]
	v_pk_add_f32 v[102:103], v[104:105], v[124:125]
	s_waitcnt vmcnt(6)
	v_lshlrev_b32_e32 v104, 16, v230
	v_and_b32_e32 v105, 0xffff0000, v230
	v_lshlrev_b32_e32 v110, 16, v231
	v_and_b32_e32 v111, 0xffff0000, v231
	v_pk_fma_f32 v[102:103], v[94:95], v[102:103], v[110:111]
	v_cvt_pk_f32_fp8_e32 v[110:111], v211
	v_pk_fma_f32 v[104:105], v[96:97], v[114:115], v[104:105]
	v_cvt_pk_f32_fp8_sdwa v[52:53], v211 src0_sel:WORD_1
	v_cvt_pk_f32_fp8_e32 v[114:115], v215
	v_cvt_pk_f32_fp8_sdwa v[56:57], v215 src0_sel:WORD_1
	v_cvt_pk_f32_fp8_sdwa v[60:61], v219 src0_sel:WORD_1
	v_cvt_pk_f32_fp8_e32 v[118:119], v223
	v_cvt_pk_f32_fp8_sdwa v[64:65], v223 src0_sel:WORD_1
	v_pk_add_f32 v[110:111], v[110:111], 0 op_sel_hi:[1,0]
	v_pk_add_f32 v[52:53], v[52:53], 0 op_sel_hi:[1,0]
	v_pk_add_f32 v[110:111], v[110:111], v[114:115]
	v_pk_add_f32 v[52:53], v[52:53], v[56:57]
	v_pk_add_f32 v[56:57], v[110:111], v[116:117]
	v_pk_add_f32 v[52:53], v[52:53], v[60:61]
	v_pk_add_f32 v[56:57], v[56:57], v[118:119]
	v_lshlrev_b32_e32 v60, 16, v232
	v_and_b32_e32 v61, 0xffff0000, v232
	v_pk_add_f32 v[52:53], v[52:53], v[64:65]
	v_lshlrev_b32_e32 v64, 16, v233
	v_and_b32_e32 v65, 0xffff0000, v233
	v_pk_fma_f32 v[56:57], v[92:93], v[56:57], v[60:61]
	v_pk_fma_f32 v[52:53], v[90:91], v[52:53], v[64:65]
	v_mov_b32_e32 v64, v105
	v_mov_b32_e32 v65, v57
	v_mov_b32_e32 v60, v104
	v_mov_b32_e32 v61, v56
	v_pk_mul_f32 v[64:65], v[64:65], v[64:65]
	v_cvt_pk_f32_fp8_sdwa v[110:111], v212 src0_sel:WORD_1
	v_pk_fma_f32 v[60:61], v[60:61], v[60:61], v[64:65]
	v_mov_b32_e32 v64, v102
	v_mov_b32_e32 v65, v52
	v_pk_fma_f32 v[60:61], v[64:65], v[64:65], v[60:61]
	v_mov_b32_e32 v64, v103
	v_mov_b32_e32 v65, v53
	v_pk_fma_f32 v[60:61], v[64:65], v[64:65], v[60:61]
	v_cvt_pk_f32_fp8_e32 v[64:65], v212
	v_cvt_pk_f32_fp8_e32 v[112:113], v216
	v_cvt_pk_f32_fp8_sdwa v[114:115], v216 src0_sel:WORD_1
	v_cvt_pk_f32_fp8_e32 v[116:117], v220
	v_cvt_pk_f32_fp8_sdwa v[118:119], v220 src0_sel:WORD_1
	v_cvt_pk_f32_fp8_e32 v[120:121], v224
	v_cvt_pk_f32_fp8_sdwa v[122:123], v224 src0_sel:WORD_1
	v_pk_add_f32 v[110:111], v[110:111], 0 op_sel_hi:[1,0]
	v_pk_add_f32 v[64:65], v[64:65], 0 op_sel_hi:[1,0]
	v_pk_add_f32 v[110:111], v[110:111], v[114:115]
	v_pk_add_f32 v[64:65], v[64:65], v[112:113]
	v_pk_add_f32 v[110:111], v[110:111], v[118:119]
	v_pk_add_f32 v[64:65], v[64:65], v[116:117]
	v_cvt_pk_f32_fp8_e32 v[114:115], v221
	v_pk_add_f32 v[112:113], v[64:65], v[120:121]
	v_pk_add_f32 v[64:65], v[110:111], v[122:123]
	v_lshlrev_b32_e32 v110, 16, v226
	v_and_b32_e32 v111, 0xffff0000, v226
	v_lshlrev_b32_e32 v68, 16, v227
	v_and_b32_e32 v69, 0xffff0000, v227
	v_pk_fma_f32 v[64:65], v[86:87], v[64:65], v[68:69]
	v_pk_fma_f32 v[68:69], v[88:89], v[112:113], v[110:111]
	v_cvt_pk_f32_fp8_e32 v[110:111], v213
	v_cvt_pk_f32_fp8_sdwa v[54:55], v213 src0_sel:WORD_1
	v_cvt_pk_f32_fp8_e32 v[112:113], v217
	v_cvt_pk_f32_fp8_sdwa v[58:59], v217 src0_sel:WORD_1
	v_cvt_pk_f32_fp8_sdwa v[62:63], v221 src0_sel:WORD_1
	v_cvt_pk_f32_fp8_e32 v[116:117], v225
	v_cvt_pk_f32_fp8_sdwa v[66:67], v225 src0_sel:WORD_1
	v_pk_add_f32 v[110:111], v[110:111], 0 op_sel_hi:[1,0]
	v_pk_add_f32 v[54:55], v[54:55], 0 op_sel_hi:[1,0]
	v_pk_add_f32 v[110:111], v[110:111], v[112:113]
	v_pk_add_f32 v[54:55], v[54:55], v[58:59]
	v_pk_add_f32 v[58:59], v[110:111], v[114:115]
	v_pk_add_f32 v[54:55], v[54:55], v[62:63]
	v_pk_add_f32 v[58:59], v[58:59], v[116:117]
	v_lshlrev_b32_e32 v62, 16, v228
	v_and_b32_e32 v63, 0xffff0000, v228
	v_pk_add_f32 v[54:55], v[54:55], v[66:67]
	v_lshlrev_b32_e32 v66, 16, v229
	v_and_b32_e32 v67, 0xffff0000, v229
	s_add_i32 vcc_lo, s21, 1
	v_readlane_b32 vcc_lo, v109, vcc_lo
	s_ashr_i32 vcc_hi, vcc_lo, 31
	s_lshl_b64 vcc, vcc, 10
	v_lshl_add_u64 v[210:211], v[72:73], 0, vcc
	global_load_dwordx4 v[210:213], v[210:211], off nt
	s_add_i32 vcc_lo, s21, 2
	v_readlane_b32 vcc_lo, v109, vcc_lo
	s_ashr_i32 vcc_hi, vcc_lo, 31
	s_lshl_b64 vcc, vcc, 10
	v_lshl_add_u64 v[214:215], v[72:73], 0, vcc
	global_load_dwordx4 v[214:217], v[214:215], off nt
	s_add_i32 vcc_lo, s21, 3
	v_readlane_b32 vcc_lo, v109, vcc_lo
	s_ashr_i32 vcc_hi, vcc_lo, 31
	s_lshl_b64 vcc, vcc, 10
	v_lshl_add_u64 v[218:219], v[72:73], 0, vcc
	global_load_dwordx4 v[218:221], v[218:219], off nt
	s_add_i32 vcc_lo, s21, 4
	v_readlane_b32 vcc_lo, v109, vcc_lo
	s_ashr_i32 vcc_hi, vcc_lo, 31
	s_lshl_b64 vcc, vcc, 10
	v_lshl_add_u64 v[222:223], v[72:73], 0, vcc
	global_load_dwordx4 v[222:225], v[222:223], off nt
	v_add_u32_e32 v236, 2, v98
	v_ashrrev_i32_e32 v237, 31, v236
	v_lshlrev_b64 v[236:237], 11, v[236:237]
	v_lshl_add_u64 v[234:235], v[74:75], 0, v[236:237]
	global_load_dwordx4 v[226:229], v[234:235], off offset:16
	global_load_dwordx4 v[230:233], v[234:235], off
	v_pk_fma_f32 v[58:59], v[84:85], v[58:59], v[62:63]
	v_pk_fma_f32 v[54:55], v[82:83], v[54:55], v[66:67]
	v_mov_b32_e32 v66, v69
	v_mov_b32_e32 v67, v59
	v_mov_b32_e32 v62, v68
	v_mov_b32_e32 v63, v58
	v_pk_mul_f32 v[66:67], v[66:67], v[66:67]
	v_add_f32_e32 v60, v60, v61
	v_pk_fma_f32 v[62:63], v[62:63], v[62:63], v[66:67]
	v_mov_b32_e32 v66, v64
	v_mov_b32_e32 v67, v54
	v_pk_fma_f32 v[62:63], v[66:67], v[66:67], v[62:63]
	v_mov_b32_e32 v66, v65
	v_mov_b32_e32 v67, v55
	v_pk_fma_f32 v[62:63], v[66:67], v[66:67], v[62:63]
	v_mbcnt_lo_u32_b32 v61, -1, 0
	v_mbcnt_hi_u32_b32 v61, -1, v61
	s_nop 0
	v_add_f32_e32 v60, v60, v62
	v_lshlrev_b32_e32 v61, 2, v61
	v_add_f32_e32 v60, v60, v63
	v_xor_b32_e32 v61, 0x80, v61
	ds_bpermute_b32 v61, v61, v60
	s_waitcnt lgkmcnt(0)
; __device__ __forceinline__ unsigned cvt_pk_bf16(float lo, float hi) { const bf16x2_t r = __builtin_convertvector((f32x2_t){lo, hi}, bf16x2_t); return __builtin_bit_cast(unsigned, r); }
; __device__ __forceinline__ float kf(float x) { asm volatile("" : "+s"(x)); return x; }
; __device__ __forceinline__ float shx(float v, int m) { int ln; asm volatile("v_mbcnt_lo_u32_b32 %0, -1, 0\n\tv_mbcnt_hi_u32_b32 %0, -1, %0" : "=v"(ln)); return __builtin_bit_cast(float, __builtin_amdgcn_ds_bpermute((ln ^ m) << 2, __builtin_bit_cast(int, v))); }
; __device__ __forceinline__ void combine_phase(LAS unsigned char* lds, const bf16_t* X, bf16_t* Xo, const unsigned char* __restrict__ YB, const float* __restrict__ mod_l, const int* __restrict__ cnt_l, ...
;     ...
;             for (int of = 32; of > 0; of >>= 1) ss += shx(ss, of);
;             const float r = rsqrtf(ss * (1.f / D) + kf(EPS));
;             if (mod_n) {
;                 u32x4 xo0, xo1, h0, h1;
;                 xo0.x = cvt_pk_bf16(v[0][0], v[0][1]); xo0.y = cvt_pk_bf16(v[0][2], v[0][3]); xo0.z = cvt_pk_bf16(v[1][0], v[1][1]); xo0.w = cvt_pk_bf16(v[1][2], v[1][3]);
;                 xo1.x = cvt_pk_bf16(v[2][0], v[2][1]); xo1.y = cvt_pk_bf16(v[2][2], v[2][3]); xo1.z = cvt_pk_bf16(v[3][0], v[3][1]); xo1.w = cvt_pk_bf16(v[3][2], v[3][3]);
;                 *(u32x4*)(Xo + (size_t)t * D + k0) = xo0; *(u32x4*)(Xo + (size_t)t * D + k0 + 8) = xo1;
;                 f32x4 o[4];
; #pragma unroll
;                 for (int q = 0; q < 4; ++q) o[q] = v[q] * r * gn[q] + sh[q];
;                 h0.x = cvt_pk_bf16(o[0][0], o[0][1]); h0.y = cvt_pk_bf16(o[0][2], o[0][3]); h0.z = cvt_pk_bf16(o[1][0], o[1][1]); h0.w = cvt_pk_bf16(o[1][2], o[1][3]);
;                 h1.x = cvt_pk_bf16(o[2][0], o[2][1]); h1.y = cvt_pk_bf16(o[2][2], o[2][3]); h1.z = cvt_pk_bf16(o[3][0], o[3][1]); h1.w = cvt_pk_bf16(o[3][2], o[3][3]);
;                 *(u32x4*)(H1B + (size_t)t * D + k0) = h0; *(u32x4*)(H1B + (size_t)t * D + k0 + 8) = h1;
	v_add_f32_e32 v60, v60, v61
	v_mbcnt_lo_u32_b32 v61, -1, 0
	v_mbcnt_hi_u32_b32 v61, -1, v61
	s_nop 0
	v_lshlrev_b32_e32 v61, 2, v61
	v_xor_b32_e32 v61, 64, v61
	ds_bpermute_b32 v61, v61, v60
	s_waitcnt lgkmcnt(0)
	v_add_f32_e32 v60, v60, v61
	v_mbcnt_lo_u32_b32 v61, -1, 0
	v_mbcnt_hi_u32_b32 v61, -1, v61
	s_nop 0
	v_lshlrev_b32_e32 v61, 2, v61
	v_xor_b32_e32 v61, 32, v61
	ds_bpermute_b32 v61, v61, v60
	s_waitcnt lgkmcnt(0)
	v_add_f32_e32 v60, v60, v61
	v_mbcnt_lo_u32_b32 v61, -1, 0
	v_mbcnt_hi_u32_b32 v61, -1, v61
	s_nop 0
	v_lshlrev_b32_e32 v61, 2, v61
	v_xor_b32_e32 v61, 16, v61
	ds_bpermute_b32 v61, v61, v60
	s_waitcnt lgkmcnt(0)
	v_add_f32_e32 v60, v60, v61
	v_mbcnt_lo_u32_b32 v61, -1, 0
	v_mbcnt_hi_u32_b32 v61, -1, v61
	s_nop 0
	v_lshlrev_b32_e32 v61, 2, v61
	v_xor_b32_e32 v61, 8, v61
	ds_bpermute_b32 v61, v61, v60
	s_waitcnt lgkmcnt(0)
	v_add_f32_e32 v60, v60, v61
	v_mbcnt_lo_u32_b32 v61, -1, 0
	v_mbcnt_hi_u32_b32 v61, -1, v61
	s_nop 0
	v_lshlrev_b32_e32 v61, 2, v61
	v_xor_b32_e32 v61, 4, v61
	ds_bpermute_b32 v61, v61, v60
	s_waitcnt lgkmcnt(0)
	v_add_f32_e32 v60, v60, v61
	v_mov_b32_e32 v61, s18
	v_fmac_f32_e32 v61, 0x3a800000, v60
	v_cmp_gt_f32_e32 vcc, s80, v61
	v_mul_f32_e32 v60, 0x4b800000, v61
	s_nop 0
	v_cndmask_b32_e32 v60, v61, v60, vcc
	v_rsq_f32_e32 v60, v60
	s_nop 0
	v_mul_f32_e32 v61, 0x45800000, v60
	v_cndmask_b32_e32 v60, v60, v61, vcc
	s_and_b64 vcc, exec, s[16:17]
	s_cbranch_vccz .LBB0_1513
	v_lshlrev_b64 v[62:63], 1, v[100:101]
	v_cvt_pk_bf16_f32 v110, v104, v105
	v_cvt_pk_bf16_f32 v111, v102, v103
	v_cvt_pk_bf16_f32 v112, v56, v57
	v_cvt_pk_bf16_f32 v113, v52, v53
	v_lshl_add_u64 v[66:67], v[76:77], 0, v[62:63]
	v_cvt_pk_bf16_f32 v114, v68, v69
	v_cvt_pk_bf16_f32 v115, v64, v65
	v_cvt_pk_bf16_f32 v116, v58, v59
	v_cvt_pk_bf16_f32 v117, v54, v55
	global_store_dwordx4 v[66:67], v[110:113], off
	global_store_dwordx4 v[66:67], v[114:117], off offset:16
	v_pk_mul_f32 v[66:67], v[102:103], v[60:61] op_sel_hi:[1,0]
	v_pk_mul_f32 v[110:111], v[52:53], v[60:61] op_sel_hi:[1,0]
	v_pk_mul_f32 v[70:71], v[104:105], v[60:61] op_sel_hi:[1,0]
	v_pk_mul_f32 v[112:113], v[56:57], v[60:61] op_sel_hi:[1,0]
	v_pk_fma_f32 v[114:115], v[32:33], v[110:111], v[20:21]
	v_pk_mul_f32 v[110:111], v[64:65], v[60:61] op_sel_hi:[1,0]
	v_pk_fma_f32 v[66:67], v[28:29], v[66:67], v[24:25]
	v_pk_fma_f32 v[70:71], v[26:27], v[70:71], v[22:23]
	v_pk_fma_f32 v[112:113], v[30:31], v[112:113], v[18:19]
	v_pk_mul_f32 v[116:117], v[68:69], v[60:61] op_sel_hi:[1,0]
	v_pk_fma_f32 v[118:119], v[46:47], v[110:111], v[42:43]
	v_pk_mul_f32 v[110:111], v[54:55], v[60:61] op_sel_hi:[1,0]
	v_pk_mul_f32 v[120:121], v[58:59], v[60:61] op_sel_hi:[1,0]
	v_pk_fma_f32 v[116:117], v[44:45], v[116:117], v[40:41]
	v_pk_fma_f32 v[122:123], v[50:51], v[110:111], v[38:39]
	v_pk_fma_f32 v[120:121], v[48:49], v[120:121], v[36:37]
	v_cvt_pk_bf16_f32 v110, v70, v71
	v_cvt_pk_bf16_f32 v111, v66, v67
	v_cvt_pk_bf16_f32 v112, v112, v113
	v_cvt_pk_bf16_f32 v113, v114, v115
	v_lshl_add_u64 v[62:63], v[78:79], 0, v[62:63]
	v_cvt_pk_bf16_f32 v114, v116, v117
	v_cvt_pk_bf16_f32 v115, v118, v119
	v_cvt_pk_bf16_f32 v116, v120, v121
	v_cvt_pk_bf16_f32 v117, v122, v123
	global_store_dwordx4 v[62:63], v[110:113], off
	global_store_dwordx4 v[62:63], v[114:117], off offset:16
	s_cbranch_execnz .LBB0_1511

; __device__ __forceinline__ float kf(float x) { asm volatile("" : "+s"(x)); return x; }
; __device__ __forceinline__ float shx(float v, int m) { int ln; asm volatile("v_mbcnt_lo_u32_b32 %0, -1, 0\n\tv_mbcnt_hi_u32_b32 %0, -1, %0" : "=v"(ln)); return __builtin_bit_cast(float, __builtin_amdgcn_ds_bpermute((ln ^ m) << 2, __builtin_bit_cast(int, v))); }
; #define YB WSP(unsigned char, W_YB)
; __device__ __forceinline__ void combine_phase(LAS unsigned char* lds, const bf16_t* X, bf16_t* Xo, const unsigned char* __restrict__ YB, const float* __restrict__ mod_l, const int* __restrict__ cnt_l, ...
;     ...
;         for (int i = 0; i < 8; ++i) {
;             const int t = t0 + i;
;             u32x4 yv[4];
; #pragma unroll
;             for (int k = 0; k < 4; ++k) { const int row = __builtin_amdgcn_readlane(rowv, i * 4 + k); yv[k] = __builtin_nontemporal_load((const u32x4*)(YB + (size_t)row * D + k0)); }
;             const u32x4 x0 = *(const u32x4*)(X + (size_t)t * D + k0), x1 = *(const u32x4*)(X + (size_t)t * D + k0 + 8);
;             f32x4 v[4]; float ss = 0.f;
; #pragma unroll
;             for (int q = 0; q < 4; ++q) {
;                 f32x4 a = (f32x4){0.f, 0.f, 0.f, 0.f};
; #pragma unroll
;                 for (int k = 0; k < 4; ++k) { const unsigned w = q == 0 ? yv[k].x : q == 1 ? yv[k].y : q == 2 ? yv[k].z : yv[k].w;
;                     const f32x2_t lo = __builtin_amdgcn_cvt_pk_f32_fp8((int)w, false), hi = __builtin_amdgcn_cvt_pk_f32_fp8((int)w, true);
;                     a[0] += lo.x; a[1] += lo.y; a[2] += hi.x; a[3] += hi.y; }
;                 const u32x4 xq = (q >> 1) ? x1 : x0; const unsigned xa = (q & 1) ? xq.z : xq.x, xb = (q & 1) ? xq.w : xq.y;
;                 v[q] = (f32x4){__uint_as_float(xa << 16), __uint_as_float(xa & 0xffff0000u), __uint_as_float(xb << 16), __uint_as_float(xb & 0xffff0000u)} + g2[q] * a;
;                 ss += v[q][0] * v[q][0] + v[q][1] * v[q][1] + v[q][2] * v[q][2] + v[q][3] * v[q][3];
;             }
;             for (int of = 32; of > 0; of >>= 1) ss += shx(ss, of);
;             const float r = rsqrtf(ss * (1.f / D) + kf(EPS));
.LBB0_1511:
	v_add_u32_e32 v68, 1, v98
	v_ashrrev_i32_e32 v69, 31, v68
	v_lshlrev_b64 v[100:101], 10, v[68:69]
	s_mov_b32 s18, 0x358637bd
	s_waitcnt vmcnt(15)
	v_cvt_pk_f32_fp8_e32 v[102:103], v182
	v_cvt_pk_f32_fp8_sdwa v[104:105], v182 src0_sel:WORD_1
	s_waitcnt vmcnt(14)
	v_cvt_pk_f32_fp8_e32 v[114:115], v186
	v_cvt_pk_f32_fp8_sdwa v[116:117], v186 src0_sel:WORD_1
	s_waitcnt vmcnt(13)
	v_cvt_pk_f32_fp8_e32 v[118:119], v190
	v_cvt_pk_f32_fp8_sdwa v[120:121], v190 src0_sel:WORD_1
	s_waitcnt vmcnt(12)
	v_cvt_pk_f32_fp8_e32 v[122:123], v194
	v_cvt_pk_f32_fp8_sdwa v[124:125], v194 src0_sel:WORD_1
	v_pk_add_f32 v[104:105], v[104:105], 0 op_sel_hi:[1,0]
	v_pk_add_f32 v[102:103], v[102:103], 0 op_sel_hi:[1,0]
	v_pk_add_f32 v[104:105], v[104:105], v[116:117]
	v_pk_add_f32 v[102:103], v[102:103], v[114:115]
	v_pk_add_f32 v[104:105], v[104:105], v[120:121]
	v_pk_add_f32 v[102:103], v[102:103], v[118:119]
	v_cvt_pk_f32_fp8_e32 v[116:117], v191
	v_pk_add_f32 v[114:115], v[102:103], v[122:123]
	v_pk_add_f32 v[102:103], v[104:105], v[124:125]
	s_waitcnt vmcnt(10)
	v_lshlrev_b32_e32 v104, 16, v202
	v_and_b32_e32 v105, 0xffff0000, v202
	v_lshlrev_b32_e32 v110, 16, v203
	v_and_b32_e32 v111, 0xffff0000, v203
	v_pk_fma_f32 v[102:103], v[94:95], v[102:103], v[110:111]
	v_cvt_pk_f32_fp8_e32 v[110:111], v183
	v_pk_fma_f32 v[104:105], v[96:97], v[114:115], v[104:105]
	v_cvt_pk_f32_fp8_sdwa v[52:53], v183 src0_sel:WORD_1
	v_cvt_pk_f32_fp8_e32 v[114:115], v187
	v_cvt_pk_f32_fp8_sdwa v[56:57], v187 src0_sel:WORD_1
	v_cvt_pk_f32_fp8_sdwa v[60:61], v191 src0_sel:WORD_1
	v_cvt_pk_f32_fp8_e32 v[118:119], v195
	v_cvt_pk_f32_fp8_sdwa v[64:65], v195 src0_sel:WORD_1
	v_pk_add_f32 v[110:111], v[110:111], 0 op_sel_hi:[1,0]
	v_pk_add_f32 v[52:53], v[52:53], 0 op_sel_hi:[1,0]
	v_pk_add_f32 v[110:111], v[110:111], v[114:115]
	v_pk_add_f32 v[52:53], v[52:53], v[56:57]
	v_pk_add_f32 v[56:57], v[110:111], v[116:117]
	v_pk_add_f32 v[52:53], v[52:53], v[60:61]
	v_pk_add_f32 v[56:57], v[56:57], v[118:119]
	v_lshlrev_b32_e32 v60, 16, v204
	v_and_b32_e32 v61, 0xffff0000, v204
	v_pk_add_f32 v[52:53], v[52:53], v[64:65]
	v_lshlrev_b32_e32 v64, 16, v205
	v_and_b32_e32 v65, 0xffff0000, v205
	v_pk_fma_f32 v[56:57], v[92:93], v[56:57], v[60:61]
	v_pk_fma_f32 v[52:53], v[90:91], v[52:53], v[64:65]
	v_mov_b32_e32 v64, v105
	v_mov_b32_e32 v65, v57
	v_mov_b32_e32 v60, v104
	v_mov_b32_e32 v61, v56
	v_pk_mul_f32 v[64:65], v[64:65], v[64:65]
	v_cvt_pk_f32_fp8_sdwa v[110:111], v184 src0_sel:WORD_1
	v_pk_fma_f32 v[60:61], v[60:61], v[60:61], v[64:65]
	v_mov_b32_e32 v64, v102
	v_mov_b32_e32 v65, v52
	v_pk_fma_f32 v[60:61], v[64:65], v[64:65], v[60:61]
	v_mov_b32_e32 v64, v103
	v_mov_b32_e32 v65, v53
	v_pk_fma_f32 v[60:61], v[64:65], v[64:65], v[60:61]
	v_cvt_pk_f32_fp8_e32 v[64:65], v184
	v_cvt_pk_f32_fp8_e32 v[112:113], v188
	v_cvt_pk_f32_fp8_sdwa v[114:115], v188 src0_sel:WORD_1
	v_cvt_pk_f32_fp8_e32 v[116:117], v192
	v_cvt_pk_f32_fp8_sdwa v[118:119], v192 src0_sel:WORD_1
	v_cvt_pk_f32_fp8_e32 v[120:121], v196
	v_cvt_pk_f32_fp8_sdwa v[122:123], v196 src0_sel:WORD_1
	v_pk_add_f32 v[110:111], v[110:111], 0 op_sel_hi:[1,0]
	v_pk_add_f32 v[64:65], v[64:65], 0 op_sel_hi:[1,0]
	v_pk_add_f32 v[110:111], v[110:111], v[114:115]
	v_pk_add_f32 v[64:65], v[64:65], v[112:113]
	v_pk_add_f32 v[110:111], v[110:111], v[118:119]
	v_pk_add_f32 v[64:65], v[64:65], v[116:117]
	v_cvt_pk_f32_fp8_e32 v[114:115], v193
	v_pk_add_f32 v[112:113], v[64:65], v[120:121]
	v_pk_add_f32 v[64:65], v[110:111], v[122:123]
	v_lshlrev_b32_e32 v110, 16, v198
	v_and_b32_e32 v111, 0xffff0000, v198
	v_lshlrev_b32_e32 v68, 16, v199
	v_and_b32_e32 v69, 0xffff0000, v199
	v_pk_fma_f32 v[64:65], v[86:87], v[64:65], v[68:69]
	v_pk_fma_f32 v[68:69], v[88:89], v[112:113], v[110:111]
	v_cvt_pk_f32_fp8_e32 v[110:111], v185
	v_cvt_pk_f32_fp8_sdwa v[54:55], v185 src0_sel:WORD_1
	v_cvt_pk_f32_fp8_e32 v[112:113], v189
	v_cvt_pk_f32_fp8_sdwa v[58:59], v189 src0_sel:WORD_1
	v_cvt_pk_f32_fp8_sdwa v[62:63], v193 src0_sel:WORD_1
	v_cvt_pk_f32_fp8_e32 v[116:117], v197
	v_cvt_pk_f32_fp8_sdwa v[66:67], v197 src0_sel:WORD_1
	v_pk_add_f32 v[110:111], v[110:111], 0 op_sel_hi:[1,0]
	v_pk_add_f32 v[54:55], v[54:55], 0 op_sel_hi:[1,0]
	v_pk_add_f32 v[110:111], v[110:111], v[112:113]
	v_pk_add_f32 v[54:55], v[54:55], v[58:59]
	v_pk_add_f32 v[58:59], v[110:111], v[114:115]
	v_pk_add_f32 v[54:55], v[54:55], v[62:63]
	v_pk_add_f32 v[58:59], v[58:59], v[116:117]
	v_lshlrev_b32_e32 v62, 16, v200
	v_and_b32_e32 v63, 0xffff0000, v200
	v_pk_add_f32 v[54:55], v[54:55], v[66:67]
	v_lshlrev_b32_e32 v66, 16, v201
	v_and_b32_e32 v67, 0xffff0000, v201
	s_add_i32 vcc_lo, s21, 5
	v_readlane_b32 vcc_lo, v109, vcc_lo
	s_ashr_i32 vcc_hi, vcc_lo, 31
	s_lshl_b64 vcc, vcc, 10
	v_lshl_add_u64 v[182:183], v[72:73], 0, vcc
	global_load_dwordx4 v[182:185], v[182:183], off nt
	s_add_i32 vcc_lo, s21, 6
	v_readlane_b32 vcc_lo, v109, vcc_lo
	s_ashr_i32 vcc_hi, vcc_lo, 31
	s_lshl_b64 vcc, vcc, 10
	v_lshl_add_u64 v[186:187], v[72:73], 0, vcc
	global_load_dwordx4 v[186:189], v[186:187], off nt
	s_add_i32 vcc_lo, s21, 7
	v_readlane_b32 vcc_lo, v109, vcc_lo
	s_ashr_i32 vcc_hi, vcc_lo, 31
	s_lshl_b64 vcc, vcc, 10
	v_lshl_add_u64 v[190:191], v[72:73], 0, vcc
	global_load_dwordx4 v[190:193], v[190:191], off nt
	s_add_i32 vcc_lo, s21, 8
	v_readlane_b32 vcc_lo, v109, vcc_lo
	s_ashr_i32 vcc_hi, vcc_lo, 31
	s_lshl_b64 vcc, vcc, 10
	v_lshl_add_u64 v[194:195], v[72:73], 0, vcc
	global_load_dwordx4 v[194:197], v[194:195], off nt
	v_add_u32_e32 v208, 3, v98
	v_ashrrev_i32_e32 v209, 31, v208
	v_lshlrev_b64 v[208:209], 11, v[208:209]
	v_lshl_add_u64 v[206:207], v[74:75], 0, v[208:209]
	global_load_dwordx4 v[198:201], v[206:207], off offset:16
	global_load_dwordx4 v[202:205], v[206:207], off
	v_pk_fma_f32 v[58:59], v[84:85], v[58:59], v[62:63]
	v_pk_fma_f32 v[54:55], v[82:83], v[54:55], v[66:67]
	v_mov_b32_e32 v66, v69
	v_mov_b32_e32 v67, v59
	v_mov_b32_e32 v62, v68
	v_mov_b32_e32 v63, v58
	v_pk_mul_f32 v[66:67], v[66:67], v[66:67]
	v_add_f32_e32 v60, v60, v61
	v_pk_fma_f32 v[62:63], v[62:63], v[62:63], v[66:67]
	v_mov_b32_e32 v66, v64
	v_mov_b32_e32 v67, v54
	v_pk_fma_f32 v[62:63], v[66:67], v[66:67], v[62:63]
	v_mov_b32_e32 v66, v65
	v_mov_b32_e32 v67, v55
	v_pk_fma_f32 v[62:63], v[66:67], v[66:67], v[62:63]
	v_mbcnt_lo_u32_b32 v61, -1, 0
	v_mbcnt_hi_u32_b32 v61, -1, v61
	s_nop 0
	v_add_f32_e32 v60, v60, v62
	v_lshlrev_b32_e32 v61, 2, v61
	v_add_f32_e32 v60, v60, v63
	v_xor_b32_e32 v61, 0x80, v61
	ds_bpermute_b32 v61, v61, v60
	s_waitcnt lgkmcnt(0)
; __device__ __forceinline__ unsigned cvt_pk_bf16(float lo, float hi) { const bf16x2_t r = __builtin_convertvector((f32x2_t){lo, hi}, bf16x2_t); return __builtin_bit_cast(unsigned, r); }
; __device__ __forceinline__ float kf(float x) { asm volatile("" : "+s"(x)); return x; }
; __device__ __forceinline__ float shx(float v, int m) { int ln; asm volatile("v_mbcnt_lo_u32_b32 %0, -1, 0\n\tv_mbcnt_hi_u32_b32 %0, -1, %0" : "=v"(ln)); return __builtin_bit_cast(float, __builtin_amdgcn_ds_bpermute((ln ^ m) << 2, __builtin_bit_cast(int, v))); }
; __device__ __forceinline__ void combine_phase(LAS unsigned char* lds, const bf16_t* X, bf16_t* Xo, const unsigned char* __restrict__ YB, const float* __restrict__ mod_l, const int* __restrict__ cnt_l, ...
;     ...
;             for (int of = 32; of > 0; of >>= 1) ss += shx(ss, of);
;             const float r = rsqrtf(ss * (1.f / D) + kf(EPS));
;             if (mod_n) {
;                 u32x4 xo0, xo1, h0, h1;
;                 xo0.x = cvt_pk_bf16(v[0][0], v[0][1]); xo0.y = cvt_pk_bf16(v[0][2], v[0][3]); xo0.z = cvt_pk_bf16(v[1][0], v[1][1]); xo0.w = cvt_pk_bf16(v[1][2], v[1][3]);
;                 xo1.x = cvt_pk_bf16(v[2][0], v[2][1]); xo1.y = cvt_pk_bf16(v[2][2], v[2][3]); xo1.z = cvt_pk_bf16(v[3][0], v[3][1]); xo1.w = cvt_pk_bf16(v[3][2], v[3][3]);
;                 *(u32x4*)(Xo + (size_t)t * D + k0) = xo0; *(u32x4*)(Xo + (size_t)t * D + k0 + 8) = xo1;
;                 f32x4 o[4];
; #pragma unroll
;                 for (int q = 0; q < 4; ++q) o[q] = v[q] * r * gn[q] + sh[q];
;                 h0.x = cvt_pk_bf16(o[0][0], o[0][1]); h0.y = cvt_pk_bf16(o[0][2], o[0][3]); h0.z = cvt_pk_bf16(o[1][0], o[1][1]); h0.w = cvt_pk_bf16(o[1][2], o[1][3]);
;                 h1.x = cvt_pk_bf16(o[2][0], o[2][1]); h1.y = cvt_pk_bf16(o[2][2], o[2][3]); h1.z = cvt_pk_bf16(o[3][0], o[3][1]); h1.w = cvt_pk_bf16(o[3][2], o[3][3]);
;                 *(u32x4*)(H1B + (size_t)t * D + k0) = h0; *(u32x4*)(H1B + (size_t)t * D + k0 + 8) = h1;
	v_add_f32_e32 v60, v60, v61
	v_mbcnt_lo_u32_b32 v61, -1, 0
	v_mbcnt_hi_u32_b32 v61, -1, v61
	s_nop 0
	v_lshlrev_b32_e32 v61, 2, v61
	v_xor_b32_e32 v61, 64, v61
	ds_bpermute_b32 v61, v61, v60
	s_waitcnt lgkmcnt(0)
	v_add_f32_e32 v60, v60, v61
	v_mbcnt_lo_u32_b32 v61, -1, 0
	v_mbcnt_hi_u32_b32 v61, -1, v61
	s_nop 0
	v_lshlrev_b32_e32 v61, 2, v61
	v_xor_b32_e32 v61, 32, v61
	ds_bpermute_b32 v61, v61, v60
	s_waitcnt lgkmcnt(0)
	v_add_f32_e32 v60, v60, v61
	v_mbcnt_lo_u32_b32 v61, -1, 0
	v_mbcnt_hi_u32_b32 v61, -1, v61
	s_nop 0
	v_lshlrev_b32_e32 v61, 2, v61
	v_xor_b32_e32 v61, 16, v61
	ds_bpermute_b32 v61, v61, v60
	s_waitcnt lgkmcnt(0)
	v_add_f32_e32 v60, v60, v61
	v_mbcnt_lo_u32_b32 v61, -1, 0
	v_mbcnt_hi_u32_b32 v61, -1, v61
	s_nop 0
	v_lshlrev_b32_e32 v61, 2, v61
	v_xor_b32_e32 v61, 8, v61
	ds_bpermute_b32 v61, v61, v60
	s_waitcnt lgkmcnt(0)
	v_add_f32_e32 v60, v60, v61
	v_mbcnt_lo_u32_b32 v61, -1, 0
	v_mbcnt_hi_u32_b32 v61, -1, v61
	s_nop 0
	v_lshlrev_b32_e32 v61, 2, v61
	v_xor_b32_e32 v61, 4, v61
	ds_bpermute_b32 v61, v61, v60
	s_waitcnt lgkmcnt(0)
	v_add_f32_e32 v60, v60, v61
	v_mov_b32_e32 v61, s18
	v_fmac_f32_e32 v61, 0x3a800000, v60
	v_cmp_gt_f32_e32 vcc, s80, v61
	v_mul_f32_e32 v60, 0x4b800000, v61
	s_nop 0
	v_cndmask_b32_e32 v60, v61, v60, vcc
	v_rsq_f32_e32 v60, v60
	s_nop 0
	v_mul_f32_e32 v61, 0x45800000, v60
	v_cndmask_b32_e32 v60, v60, v61, vcc
	s_and_b64 vcc, exec, s[6:7]
	s_cbranch_vccnz .LBB0_1514
	v_lshlrev_b64 v[62:63], 1, v[100:101]
	v_cvt_pk_bf16_f32 v110, v104, v105
	v_cvt_pk_bf16_f32 v111, v102, v103
	v_cvt_pk_bf16_f32 v112, v56, v57
	v_cvt_pk_bf16_f32 v113, v52, v53
	v_lshl_add_u64 v[66:67], v[76:77], 0, v[62:63]
	v_cvt_pk_bf16_f32 v114, v68, v69
	v_cvt_pk_bf16_f32 v115, v64, v65
	v_cvt_pk_bf16_f32 v116, v58, v59
	v_cvt_pk_bf16_f32 v117, v54, v55
	global_store_dwordx4 v[66:67], v[110:113], off
	global_store_dwordx4 v[66:67], v[114:117], off offset:16
	v_pk_mul_f32 v[66:67], v[102:103], v[60:61] op_sel_hi:[1,0]
	v_pk_mul_f32 v[110:111], v[52:53], v[60:61] op_sel_hi:[1,0]
	v_pk_mul_f32 v[70:71], v[104:105], v[60:61] op_sel_hi:[1,0]
	v_pk_mul_f32 v[112:113], v[56:57], v[60:61] op_sel_hi:[1,0]
	v_pk_fma_f32 v[114:115], v[32:33], v[110:111], v[20:21]
	v_pk_mul_f32 v[110:111], v[64:65], v[60:61] op_sel_hi:[1,0]
	v_pk_fma_f32 v[66:67], v[28:29], v[66:67], v[24:25]
	v_pk_fma_f32 v[70:71], v[26:27], v[70:71], v[22:23]
	v_pk_fma_f32 v[112:113], v[30:31], v[112:113], v[18:19]
	v_pk_mul_f32 v[116:117], v[68:69], v[60:61] op_sel_hi:[1,0]
	v_pk_fma_f32 v[118:119], v[46:47], v[110:111], v[42:43]
	v_pk_mul_f32 v[110:111], v[54:55], v[60:61] op_sel_hi:[1,0]
	v_pk_mul_f32 v[120:121], v[58:59], v[60:61] op_sel_hi:[1,0]
	v_pk_fma_f32 v[116:117], v[44:45], v[116:117], v[40:41]
	v_pk_fma_f32 v[122:123], v[50:51], v[110:111], v[38:39]
	v_pk_fma_f32 v[120:121], v[48:49], v[120:121], v[36:37]
	v_cvt_pk_bf16_f32 v110, v70, v71
	v_cvt_pk_bf16_f32 v111, v66, v67
	v_cvt_pk_bf16_f32 v112, v112, v113
	v_cvt_pk_bf16_f32 v113, v114, v115
	v_lshl_add_u64 v[62:63], v[78:79], 0, v[62:63]
	v_cvt_pk_bf16_f32 v114, v116, v117
	v_cvt_pk_bf16_f32 v115, v118, v119
	v_cvt_pk_bf16_f32 v116, v120, v121
	v_cvt_pk_bf16_f32 v117, v122, v123
	global_store_dwordx4 v[62:63], v[110:113], off
	global_store_dwordx4 v[62:63], v[114:117], off offset:16
	s_cbranch_execnz .LBB0_1507
	s_branch .LBB0_1506
